# v78 with the baseline's nt policy restored on the 16 SwiGLU activation stores
# speedup vs baseline: 1.0022x; 1.0022x over previous
; __device__ __forceinline__ unsigned cvt_pk4_fp8(float a, float b, float c, float d) { int w = 0; w = __builtin_amdgcn_cvt_pk_fp8_f32(a, b, w, false); w = __builtin_amdgcn_cvt_pk_fp8_f32(c, d, w, true); return (unsigned)w; }
; __device__ __forceinline__ unsigned cvt_pk_bf16(float lo, float hi) { unsigned r; asm volatile("v_cvt_pk_bf16_f32 %0, %1, %2" : "=v"(r) : "v"(lo), "v"(hi)); return r; }
; __device__ __forceinline__ f32x2p silu_mul2k(f32x2p ag, f32x2p au, float kt, float ci) { const f32x2p t = ag * kt; f32x2p e; e.x = __builtin_amdgcn_exp2f(t.x); e.y = __builtin_amdgcn_exp2f(t.y);
;     const f32x2p d = e * ci + ci; f32x2p r; r.x = __builtin_amdgcn_rcpf(d.x); r.y = __builtin_amdgcn_rcpf(d.y); return (ag * au) * r; }
;     __device__ __forceinline__ void operator()(const f32x4 (&acc)[2][2][4][2], const Unit& u, int wr, int wc, int fr, int fq) const {
;     ...
;             for (int m = 0; m < 4; ++m) { const size_t off = (size_t)(row0 + ai * HALF + m * 16) * ldc + col0;
;                 const f32x4 g0 = acc[ai][0][m][0], g1 = acc[ai][0][m][1], u0 = acc[ai][1][m][0], u1 = acc[ai][1][m][1];
;                 float v[8];
;                 { const f32x2p a = silu_mul2k((f32x2p){g0[0], g0[1]}, (f32x2p){u0[0], u0[1]}, kt, ci), b = silu_mul2k((f32x2p){g0[2], g0[3]}, (f32x2p){u0[2], u0[3]}, kt, ci), c = silu_mul2k((f32x2p){g1[0], g1[1]}, (f32x2p){u1[0], u1[1]}, kt, ci), d = silu_mul2k((f32x2p){g1[2], g1[3]}, (f32x2p){u1[2], u1[3]}, kt, ci);
;                   v[0] = a.x; v[1] = a.y; v[2] = b.x; v[3] = b.y; v[4] = c.x; v[5] = c.y; v[6] = d.x; v[7] = d.y; }
;                 if constexpr (FP8OUT) { typedef unsigned u32x2 __attribute__((ext_vector_type(2))); u32x2 w; w.x = cvt_pk4_fp8(v[0], v[1], v[2], v[3]); w.y = cvt_pk4_fp8(v[4], v[5], v[6], v[7]); __builtin_nontemporal_store(w, (u32x2*)((unsigned char*)O + off)); }
;                 else { u32x4 w; w.x = cvt_pk_bf16(v[0], v[1]); w.y = cvt_pk_bf16(v[2], v[3]); w.z = cvt_pk_bf16(v[4], v[5]); w.w = cvt_pk_bf16(v[6], v[7]); __builtin_nontemporal_store(w, (u32x4*)((bf16_t*)O + off)); } }
.LBB0_870:
	v_pk_mul_f32 v[0:1], v[156:157], s[16:17] op_sel_hi:[1,0]
	v_pk_mul_f32 v[8:9], v[156:157], v[124:125]
	v_exp_f32_e32 v2, v0
	v_exp_f32_e32 v3, v1
	v_pk_mul_f32 v[10:11], v[152:153], s[16:17] op_sel_hi:[1,0]
	v_pk_mul_f32 v[12:13], v[154:155], s[16:17] op_sel_hi:[1,0]
	v_exp_f32_e32 v10, v10
	v_pk_fma_f32 v[2:3], v[2:3], s[22:23], s[22:23] op_sel_hi:[1,0,0]
	v_exp_f32_e32 v11, v11
	v_rcp_f32_e32 v2, v2
	v_rcp_f32_e32 v3, v3
	v_exp_f32_e32 v12, v12
	v_pk_fma_f32 v[10:11], v[10:11], s[22:23], s[22:23] op_sel_hi:[1,0,0]
	v_exp_f32_e32 v13, v13
	v_pk_mul_f32 v[2:3], v[8:9], v[2:3]
	v_pk_mul_f32 v[8:9], v[158:159], s[16:17] op_sel_hi:[1,0]
	v_rcp_f32_e32 v10, v10
	v_exp_f32_e32 v8, v8
	v_exp_f32_e32 v9, v9
	v_rcp_f32_e32 v11, v11
	v_pk_mul_f32 v[6:7], v[158:159], v[126:127]
	v_add_u32_e32 v4, s61, v184
	v_pk_fma_f32 v[8:9], v[8:9], s[22:23], s[22:23] op_sel_hi:[1,0,0]
	v_lshl_add_u32 v0, s62, 7, v186
	v_rcp_f32_e32 v8, v8
	v_rcp_f32_e32 v9, v9
	v_ashrrev_i32_e32 v1, 31, v0
	s_nop 15
	s_nop 15
	v_pk_mul_f32 v[14:15], v[146:147], s[16:17] op_sel_hi:[1,0]
	v_pk_mul_f32 v[6:7], v[6:7], v[8:9]
	v_pk_mul_f32 v[8:9], v[152:153], v[120:121]
	v_exp_f32_e32 v14, v14
	v_pk_mul_f32 v[8:9], v[8:9], v[10:11]
	v_pk_fma_f32 v[10:11], v[12:13], s[22:23], s[22:23] op_sel_hi:[1,0,0]
	v_cvt_pk_fp8_f32 v12, v2, v3
	v_rcp_f32_e32 v10, v10
	v_rcp_f32_e32 v11, v11
	v_cvt_pk_fp8_f32 v12, v6, v7 op_sel:[0,0,1]
	v_pk_mul_f32 v[6:7], v[148:149], s[16:17] op_sel_hi:[1,0]
	v_cvt_pk_fp8_f32 v13, v8, v9
	v_exp_f32_e32 v6, v6
	v_exp_f32_e32 v7, v7
	v_pk_mul_f32 v[2:3], v[154:155], v[122:123]
	v_exp_f32_e32 v15, v15
	v_pk_mul_f32 v[2:3], v[2:3], v[10:11]
	v_pk_fma_f32 v[6:7], v[6:7], s[22:23], s[22:23] op_sel_hi:[1,0,0]
	v_cvt_pk_fp8_f32 v13, v2, v3 op_sel:[0,0,1]
	v_rcp_f32_e32 v6, v6
	v_rcp_f32_e32 v7, v7
	v_mov_b64_e32 v[2:3], s[20:21]
	v_mad_i64_i32 v[8:9], s[44:45], v4, s58, v[2:3]
	v_pk_mul_f32 v[10:11], v[148:149], v[116:117]
	v_lshl_add_u64 v[8:9], v[8:9], 0, v[0:1]
	v_pk_mul_f32 v[6:7], v[10:11], v[6:7]
	v_pk_mul_f32 v[10:11], v[150:151], s[16:17] op_sel_hi:[1,0]
	global_store_dwordx2 v[8:9], v[12:13], off nt
	v_exp_f32_e32 v10, v10
	v_exp_f32_e32 v11, v11
	v_pk_mul_f32 v[12:13], v[144:145], s[16:17] op_sel_hi:[1,0]
	v_pk_mul_f32 v[8:9], v[150:151], v[118:119]
	v_exp_f32_e32 v12, v12
	v_exp_f32_e32 v13, v13
	v_pk_fma_f32 v[10:11], v[10:11], s[22:23], s[22:23] op_sel_hi:[1,0,0]
	v_add_u32_e32 v5, 16, v4
	v_rcp_f32_e32 v10, v10
	v_rcp_f32_e32 v11, v11
	v_pk_fma_f32 v[12:13], v[12:13], s[22:23], s[22:23] op_sel_hi:[1,0,0]
	v_readlane_b32 s68, v254, 28
	v_rcp_f32_e32 v12, v12
	v_rcp_f32_e32 v13, v13
	v_pk_mul_f32 v[8:9], v[8:9], v[10:11]
	v_pk_mul_f32 v[10:11], v[144:145], v[112:113]
	s_andn2_b64 vcc, exec, s[8:9]
	v_pk_mul_f32 v[10:11], v[10:11], v[12:13]
	v_pk_fma_f32 v[12:13], v[14:15], s[22:23], s[22:23] op_sel_hi:[1,0,0]
	v_rcp_f32_e32 v12, v12
	v_rcp_f32_e32 v13, v13
	v_cvt_pk_fp8_f32 v15, v10, v11
	v_cvt_pk_fp8_f32 v14, v6, v7
	v_pk_mul_f32 v[6:7], v[146:147], v[114:115]
	v_pk_mul_f32 v[10:11], v[140:141], v[108:109]
	v_pk_mul_f32 v[6:7], v[6:7], v[12:13]
	v_pk_mul_f32 v[12:13], v[136:137], s[16:17] op_sel_hi:[1,0]
	v_cvt_pk_fp8_f32 v15, v6, v7 op_sel:[0,0,1]
	v_pk_mul_f32 v[6:7], v[140:141], s[16:17] op_sel_hi:[1,0]
	v_cvt_pk_fp8_f32 v14, v8, v9 op_sel:[0,0,1]
	v_exp_f32_e32 v6, v6
	v_exp_f32_e32 v7, v7
	v_exp_f32_e32 v12, v12
	v_exp_f32_e32 v13, v13
	v_mad_i64_i32 v[8:9], s[44:45], v5, s58, v[2:3]
	v_pk_fma_f32 v[6:7], v[6:7], s[22:23], s[22:23] op_sel_hi:[1,0,0]
	v_lshl_add_u64 v[8:9], v[8:9], 0, v[0:1]
	v_rcp_f32_e32 v6, v6
	v_rcp_f32_e32 v7, v7
	global_store_dwordx2 v[8:9], v[14:15], off nt
	v_pk_fma_f32 v[12:13], v[12:13], s[22:23], s[22:23] op_sel_hi:[1,0,0]
	v_pk_mul_f32 v[14:15], v[138:139], s[16:17] op_sel_hi:[1,0]
	v_pk_mul_f32 v[6:7], v[10:11], v[6:7]
	v_pk_mul_f32 v[10:11], v[142:143], s[16:17] op_sel_hi:[1,0]
	v_rcp_f32_e32 v12, v12
	v_exp_f32_e32 v10, v10
	v_exp_f32_e32 v11, v11
	v_rcp_f32_e32 v13, v13
	v_exp_f32_e32 v14, v14
	v_exp_f32_e32 v15, v15
	v_pk_fma_f32 v[10:11], v[10:11], s[22:23], s[22:23] op_sel_hi:[1,0,0]
	v_pk_mul_f32 v[8:9], v[142:143], v[110:111]
	v_rcp_f32_e32 v10, v10
	v_rcp_f32_e32 v11, v11
	v_add_u32_e32 v5, 32, v4
	s_mov_b64 s[8:9], -1
	v_readlane_b32 s69, v254, 29
	v_pk_mul_f32 v[8:9], v[8:9], v[10:11]
	v_pk_mul_f32 v[10:11], v[136:137], v[104:105]
	v_readlane_b32 s70, v254, 30
	v_pk_mul_f32 v[10:11], v[10:11], v[12:13]
	v_pk_fma_f32 v[12:13], v[14:15], s[22:23], s[22:23] op_sel_hi:[1,0,0]
	v_rcp_f32_e32 v12, v12
	v_rcp_f32_e32 v13, v13
	v_cvt_pk_fp8_f32 v15, v10, v11
	v_cvt_pk_fp8_f32 v14, v6, v7
	v_pk_mul_f32 v[6:7], v[138:139], v[106:107]
	v_pk_mul_f32 v[10:11], v[132:133], v[100:101]
	v_pk_mul_f32 v[6:7], v[6:7], v[12:13]
	v_pk_mul_f32 v[12:13], v[128:129], s[16:17] op_sel_hi:[1,0]
	v_cvt_pk_fp8_f32 v15, v6, v7 op_sel:[0,0,1]
	v_pk_mul_f32 v[6:7], v[132:133], s[16:17] op_sel_hi:[1,0]
	v_cvt_pk_fp8_f32 v14, v8, v9 op_sel:[0,0,1]
	v_exp_f32_e32 v6, v6
	v_exp_f32_e32 v7, v7
	v_exp_f32_e32 v12, v12
	v_exp_f32_e32 v13, v13
	v_mad_i64_i32 v[8:9], s[44:45], v5, s58, v[2:3]
	v_pk_fma_f32 v[6:7], v[6:7], s[22:23], s[22:23] op_sel_hi:[1,0,0]
	v_lshl_add_u64 v[8:9], v[8:9], 0, v[0:1]
	v_rcp_f32_e32 v6, v6
	v_rcp_f32_e32 v7, v7
	global_store_dwordx2 v[8:9], v[14:15], off nt
	v_pk_fma_f32 v[12:13], v[12:13], s[22:23], s[22:23] op_sel_hi:[1,0,0]
	v_pk_mul_f32 v[14:15], v[130:131], s[16:17] op_sel_hi:[1,0]
	v_pk_mul_f32 v[6:7], v[10:11], v[6:7]
	v_pk_mul_f32 v[10:11], v[134:135], s[16:17] op_sel_hi:[1,0]
	v_rcp_f32_e32 v12, v12
	v_exp_f32_e32 v10, v10
	v_exp_f32_e32 v11, v11
	v_rcp_f32_e32 v13, v13
	v_exp_f32_e32 v14, v14
; __device__ __forceinline__ unsigned cvt_pk4_fp8(float a, float b, float c, float d) { int w = 0; w = __builtin_amdgcn_cvt_pk_fp8_f32(a, b, w, false); w = __builtin_amdgcn_cvt_pk_fp8_f32(c, d, w, true); return (unsigned)w; }
; __device__ __forceinline__ unsigned cvt_pk_bf16(float lo, float hi) { unsigned r; asm volatile("v_cvt_pk_bf16_f32 %0, %1, %2" : "=v"(r) : "v"(lo), "v"(hi)); return r; }
; __device__ __forceinline__ f32x2p silu_mul2k(f32x2p ag, f32x2p au, float kt, float ci) { const f32x2p t = ag * kt; f32x2p e; e.x = __builtin_amdgcn_exp2f(t.x); e.y = __builtin_amdgcn_exp2f(t.y);
;     const f32x2p d = e * ci + ci; f32x2p r; r.x = __builtin_amdgcn_rcpf(d.x); r.y = __builtin_amdgcn_rcpf(d.y); return (ag * au) * r; }
;     __device__ __forceinline__ void operator()(const f32x4 (&acc)[2][2][4][2], const Unit& u, int wr, int wc, int fr, int fq) const {
;     ...
;             for (int m = 0; m < 4; ++m) { const size_t off = (size_t)(row0 + ai * HALF + m * 16) * ldc + col0;
;                 const f32x4 g0 = acc[ai][0][m][0], g1 = acc[ai][0][m][1], u0 = acc[ai][1][m][0], u1 = acc[ai][1][m][1];
;                 float v[8];
;                 { const f32x2p a = silu_mul2k((f32x2p){g0[0], g0[1]}, (f32x2p){u0[0], u0[1]}, kt, ci), b = silu_mul2k((f32x2p){g0[2], g0[3]}, (f32x2p){u0[2], u0[3]}, kt, ci), c = silu_mul2k((f32x2p){g1[0], g1[1]}, (f32x2p){u1[0], u1[1]}, kt, ci), d = silu_mul2k((f32x2p){g1[2], g1[3]}, (f32x2p){u1[2], u1[3]}, kt, ci);
;                   v[0] = a.x; v[1] = a.y; v[2] = b.x; v[3] = b.y; v[4] = c.x; v[5] = c.y; v[6] = d.x; v[7] = d.y; }
;                 if constexpr (FP8OUT) { typedef unsigned u32x2 __attribute__((ext_vector_type(2))); u32x2 w; w.x = cvt_pk4_fp8(v[0], v[1], v[2], v[3]); w.y = cvt_pk4_fp8(v[4], v[5], v[6], v[7]); __builtin_nontemporal_store(w, (u32x2*)((unsigned char*)O + off)); }
;                 else { u32x4 w; w.x = cvt_pk_bf16(v[0], v[1]); w.y = cvt_pk_bf16(v[2], v[3]); w.z = cvt_pk_bf16(v[4], v[5]); w.w = cvt_pk_bf16(v[6], v[7]); __builtin_nontemporal_store(w, (u32x4*)((bf16_t*)O + off)); } }
	v_exp_f32_e32 v15, v15
	v_pk_fma_f32 v[10:11], v[10:11], s[22:23], s[22:23] op_sel_hi:[1,0,0]
	v_pk_mul_f32 v[8:9], v[134:135], v[102:103]
	v_rcp_f32_e32 v10, v10
	v_rcp_f32_e32 v11, v11
	v_add_u32_e32 v5, 48, v4
	v_readlane_b32 s71, v254, 31
	v_readlane_b32 s72, v254, 32
	v_pk_mul_f32 v[8:9], v[8:9], v[10:11]
	v_pk_mul_f32 v[10:11], v[128:129], v[96:97]
	v_readlane_b32 s73, v254, 33
	v_pk_mul_f32 v[10:11], v[10:11], v[12:13]
	v_pk_fma_f32 v[12:13], v[14:15], s[22:23], s[22:23] op_sel_hi:[1,0,0]
	v_rcp_f32_e32 v12, v12
	v_rcp_f32_e32 v13, v13
	v_cvt_pk_fp8_f32 v15, v10, v11
	v_cvt_pk_fp8_f32 v14, v6, v7
	v_pk_mul_f32 v[6:7], v[130:131], v[98:99]
	v_pk_mul_f32 v[10:11], v[92:93], v[60:61]
	v_pk_mul_f32 v[6:7], v[6:7], v[12:13]
	v_pk_mul_f32 v[12:13], v[88:89], s[16:17] op_sel_hi:[1,0]
	v_cvt_pk_fp8_f32 v15, v6, v7 op_sel:[0,0,1]
	v_pk_mul_f32 v[6:7], v[92:93], s[16:17] op_sel_hi:[1,0]
	v_cvt_pk_fp8_f32 v14, v8, v9 op_sel:[0,0,1]
	v_exp_f32_e32 v6, v6
	v_exp_f32_e32 v7, v7
	v_exp_f32_e32 v12, v12
	v_exp_f32_e32 v13, v13
	v_mad_i64_i32 v[8:9], s[44:45], v5, s58, v[2:3]
	v_pk_fma_f32 v[6:7], v[6:7], s[22:23], s[22:23] op_sel_hi:[1,0,0]
	v_lshl_add_u64 v[8:9], v[8:9], 0, v[0:1]
	v_rcp_f32_e32 v6, v6
	v_rcp_f32_e32 v7, v7
	global_store_dwordx2 v[8:9], v[14:15], off nt
	v_pk_fma_f32 v[12:13], v[12:13], s[22:23], s[22:23] op_sel_hi:[1,0,0]
	v_pk_mul_f32 v[14:15], v[90:91], s[16:17] op_sel_hi:[1,0]
	v_pk_mul_f32 v[6:7], v[10:11], v[6:7]
	v_pk_mul_f32 v[10:11], v[94:95], s[16:17] op_sel_hi:[1,0]
	v_rcp_f32_e32 v12, v12
	v_exp_f32_e32 v10, v10
	v_exp_f32_e32 v11, v11
	v_rcp_f32_e32 v13, v13
	v_exp_f32_e32 v14, v14
	v_exp_f32_e32 v15, v15
	v_pk_fma_f32 v[10:11], v[10:11], s[22:23], s[22:23] op_sel_hi:[1,0,0]
	v_pk_mul_f32 v[8:9], v[94:95], v[62:63]
	v_rcp_f32_e32 v10, v10
	v_rcp_f32_e32 v11, v11
	v_add_u32_e32 v5, 0x80, v4
	v_readlane_b32 s74, v254, 34
	v_readlane_b32 s75, v254, 35
	v_pk_mul_f32 v[8:9], v[8:9], v[10:11]
	v_pk_mul_f32 v[10:11], v[88:89], v[56:57]
	s_nop 0
	v_pk_mul_f32 v[10:11], v[10:11], v[12:13]
	v_pk_fma_f32 v[12:13], v[14:15], s[22:23], s[22:23] op_sel_hi:[1,0,0]
	v_rcp_f32_e32 v12, v12
	v_rcp_f32_e32 v13, v13
	v_cvt_pk_fp8_f32 v15, v10, v11
	v_cvt_pk_fp8_f32 v14, v6, v7
	v_pk_mul_f32 v[6:7], v[90:91], v[58:59]
	v_pk_mul_f32 v[10:11], v[84:85], v[52:53]
	v_pk_mul_f32 v[6:7], v[6:7], v[12:13]
	v_pk_mul_f32 v[12:13], v[80:81], s[16:17] op_sel_hi:[1,0]
	v_cvt_pk_fp8_f32 v15, v6, v7 op_sel:[0,0,1]
	v_pk_mul_f32 v[6:7], v[84:85], s[16:17] op_sel_hi:[1,0]
	v_cvt_pk_fp8_f32 v14, v8, v9 op_sel:[0,0,1]
	v_exp_f32_e32 v6, v6
	v_exp_f32_e32 v7, v7
	v_exp_f32_e32 v12, v12
	v_exp_f32_e32 v13, v13
	v_mad_i64_i32 v[8:9], s[44:45], v5, s58, v[2:3]
	v_pk_fma_f32 v[6:7], v[6:7], s[22:23], s[22:23] op_sel_hi:[1,0,0]
	v_lshl_add_u64 v[8:9], v[8:9], 0, v[0:1]
	v_rcp_f32_e32 v6, v6
	v_rcp_f32_e32 v7, v7
	global_store_dwordx2 v[8:9], v[14:15], off nt
	v_pk_fma_f32 v[12:13], v[12:13], s[22:23], s[22:23] op_sel_hi:[1,0,0]
	v_pk_mul_f32 v[14:15], v[82:83], s[16:17] op_sel_hi:[1,0]
	v_pk_mul_f32 v[6:7], v[10:11], v[6:7]
	v_pk_mul_f32 v[10:11], v[86:87], s[16:17] op_sel_hi:[1,0]
	v_rcp_f32_e32 v12, v12
	v_exp_f32_e32 v10, v10
	v_exp_f32_e32 v11, v11
	v_rcp_f32_e32 v13, v13
	v_exp_f32_e32 v14, v14
	v_exp_f32_e32 v15, v15
	v_pk_fma_f32 v[10:11], v[10:11], s[22:23], s[22:23] op_sel_hi:[1,0,0]
	v_pk_mul_f32 v[8:9], v[86:87], v[54:55]
	v_rcp_f32_e32 v10, v10
	v_rcp_f32_e32 v11, v11
	v_add_u32_e32 v5, 0x90, v4
	v_pk_mul_f32 v[8:9], v[8:9], v[10:11]
	v_pk_mul_f32 v[10:11], v[80:81], v[48:49]
	s_nop 0
	v_pk_mul_f32 v[10:11], v[10:11], v[12:13]
	v_pk_fma_f32 v[12:13], v[14:15], s[22:23], s[22:23] op_sel_hi:[1,0,0]
; __device__ __forceinline__ unsigned cvt_pk4_fp8(float a, float b, float c, float d) { int w = 0; w = __builtin_amdgcn_cvt_pk_fp8_f32(a, b, w, false); w = __builtin_amdgcn_cvt_pk_fp8_f32(c, d, w, true); return (unsigned)w; }
;     __device__ __forceinline__ void operator()(const f32x4 (&acc)[2][2][4][2], const Unit& u, int wr, int wc, int fr, int fq) const {
;     ...
;             for (int m = 0; m < 4; ++m) { const size_t off = (size_t)(row0 + ai * HALF + m * 16) * ldc + col0;
;                 const f32x4 g0 = acc[ai][0][m][0], g1 = acc[ai][0][m][1], u0 = acc[ai][1][m][0], u1 = acc[ai][1][m][1];
;                 float v[8];
;                 { const f32x2p a = silu_mul2k((f32x2p){g0[0], g0[1]}, (f32x2p){u0[0], u0[1]}, kt, ci), b = silu_mul2k((f32x2p){g0[2], g0[3]}, (f32x2p){u0[2], u0[3]}, kt, ci), c = silu_mul2k((f32x2p){g1[0], g1[1]}, (f32x2p){u1[0], u1[1]}, kt, ci), d = silu_mul2k((f32x2p){g1[2], g1[3]}, (f32x2p){u1[2], u1[3]}, kt, ci);
;                   v[0] = a.x; v[1] = a.y; v[2] = b.x; v[3] = b.y; v[4] = c.x; v[5] = c.y; v[6] = d.x; v[7] = d.y; }
;                 if constexpr (FP8OUT) { typedef unsigned u32x2 __attribute__((ext_vector_type(2))); u32x2 w; w.x = cvt_pk4_fp8(v[0], v[1], v[2], v[3]); w.y = cvt_pk4_fp8(v[4], v[5], v[6], v[7]); __builtin_nontemporal_store(w, (u32x2*)((unsigned char*)O + off)); }
;                 else { u32x4 w; w.x = cvt_pk_bf16(v[0], v[1]); w.y = cvt_pk_bf16(v[2], v[3]); w.z = cvt_pk_bf16(v[4], v[5]); w.w = cvt_pk_bf16(v[6], v[7]); __builtin_nontemporal_store(w, (u32x4*)((bf16_t*)O + off)); } }
; template <class Epi, class Sched, bool ALIGN_EPI = false, bool SP2 = false, bool FP8 = false, bool PEEL = false>
; __device__ __forceinline__ void gemm_phase(PG8_LAS unsigned char* lds, const Gemm g, const Sched& S, const Epi& E, const int wid) {
;     ...
;         if constexpr (!Epi::AFTER_DRAIN) { E(acc, cur, wr, wc, fr, fq); S.done(cur); }
;         if (!has_next) break;
;         if constexpr (!PEEL) {
; #pragma unroll
;         for (int a = 0; a < 2; ++a)
; #pragma unroll
;             for (int b = 0; b < 2; ++b)
; #pragma unroll
;                 for (int m = 0; m < 4; ++m)
; #pragma unroll
;                     for (int n = 0; n < 2; ++n) acc[a][b][m][n] = (f32x4){0.f, 0.f, 0.f, 0.f};
;         }
;         cur = nxt; cA = nA; cB = nB; ++ui;
;         if constexpr (ALIGN_EPI) { if (wr == 1) PG8_BAR; }
	v_rcp_f32_e32 v12, v12
	v_rcp_f32_e32 v13, v13
	v_cvt_pk_fp8_f32 v15, v10, v11
	v_cvt_pk_fp8_f32 v14, v6, v7
	v_pk_mul_f32 v[6:7], v[82:83], v[50:51]
	v_pk_mul_f32 v[10:11], v[76:77], v[44:45]
	v_pk_mul_f32 v[6:7], v[6:7], v[12:13]
	v_pk_mul_f32 v[12:13], v[72:73], s[16:17] op_sel_hi:[1,0]
	v_cvt_pk_fp8_f32 v15, v6, v7 op_sel:[0,0,1]
	v_pk_mul_f32 v[6:7], v[76:77], s[16:17] op_sel_hi:[1,0]
	v_cvt_pk_fp8_f32 v14, v8, v9 op_sel:[0,0,1]
	v_exp_f32_e32 v6, v6
	v_exp_f32_e32 v7, v7
	v_exp_f32_e32 v12, v12
	v_exp_f32_e32 v13, v13
	v_mad_i64_i32 v[8:9], s[44:45], v5, s58, v[2:3]
	v_pk_fma_f32 v[6:7], v[6:7], s[22:23], s[22:23] op_sel_hi:[1,0,0]
	v_lshl_add_u64 v[8:9], v[8:9], 0, v[0:1]
	v_rcp_f32_e32 v6, v6
	v_rcp_f32_e32 v7, v7
	global_store_dwordx2 v[8:9], v[14:15], off nt
	v_pk_fma_f32 v[12:13], v[12:13], s[22:23], s[22:23] op_sel_hi:[1,0,0]
	v_pk_mul_f32 v[14:15], v[74:75], s[16:17] op_sel_hi:[1,0]
	v_pk_mul_f32 v[6:7], v[10:11], v[6:7]
	v_pk_mul_f32 v[10:11], v[78:79], s[16:17] op_sel_hi:[1,0]
	v_rcp_f32_e32 v12, v12
	v_exp_f32_e32 v10, v10
	v_exp_f32_e32 v11, v11
	v_rcp_f32_e32 v13, v13
	v_exp_f32_e32 v14, v14
	v_exp_f32_e32 v15, v15
	v_pk_fma_f32 v[10:11], v[10:11], s[22:23], s[22:23] op_sel_hi:[1,0,0]
	v_pk_mul_f32 v[8:9], v[78:79], v[46:47]
	v_rcp_f32_e32 v10, v10
	v_rcp_f32_e32 v11, v11
	v_add_u32_e32 v5, 0xa0, v4
	v_pk_mul_f32 v[8:9], v[8:9], v[10:11]
	v_pk_mul_f32 v[10:11], v[72:73], v[40:41]
	s_nop 0
	v_pk_mul_f32 v[10:11], v[10:11], v[12:13]
	v_pk_fma_f32 v[12:13], v[14:15], s[22:23], s[22:23] op_sel_hi:[1,0,0]
	v_rcp_f32_e32 v12, v12
	v_rcp_f32_e32 v13, v13
	v_cvt_pk_fp8_f32 v15, v10, v11
	v_cvt_pk_fp8_f32 v14, v6, v7
	v_pk_mul_f32 v[6:7], v[74:75], v[42:43]
	v_pk_mul_f32 v[10:11], v[64:65], s[16:17] op_sel_hi:[1,0]
	v_pk_mul_f32 v[6:7], v[6:7], v[12:13]
	v_cvt_pk_fp8_f32 v14, v8, v9 op_sel:[0,0,1]
	v_cvt_pk_fp8_f32 v15, v6, v7 op_sel:[0,0,1]
	v_pk_mul_f32 v[6:7], v[68:69], s[16:17] op_sel_hi:[1,0]
	v_mad_i64_i32 v[8:9], s[44:45], v5, s58, v[2:3]
	v_exp_f32_e32 v6, v6
	v_exp_f32_e32 v7, v7
	v_lshl_add_u64 v[8:9], v[8:9], 0, v[0:1]
	global_store_dwordx2 v[8:9], v[14:15], off nt
	v_pk_mul_f32 v[8:9], v[68:69], v[36:37]
	v_pk_fma_f32 v[6:7], v[6:7], s[22:23], s[22:23] op_sel_hi:[1,0,0]
	v_exp_f32_e32 v10, v10
	v_rcp_f32_e32 v6, v6
	v_rcp_f32_e32 v7, v7
	v_exp_f32_e32 v11, v11
	v_pk_mul_f32 v[12:13], v[66:67], s[16:17] op_sel_hi:[1,0]
	v_add_u32_e32 v14, 0xb0, v4
	v_pk_mul_f32 v[6:7], v[8:9], v[6:7]
	v_pk_mul_f32 v[8:9], v[70:71], s[16:17] op_sel_hi:[1,0]
	v_pk_fma_f32 v[10:11], v[10:11], s[22:23], s[22:23] op_sel_hi:[1,0,0]
	v_exp_f32_e32 v8, v8
	v_exp_f32_e32 v9, v9
	v_rcp_f32_e32 v10, v10
	v_rcp_f32_e32 v11, v11
	v_exp_f32_e32 v12, v12
	v_pk_fma_f32 v[8:9], v[8:9], s[22:23], s[22:23] op_sel_hi:[1,0,0]
	v_exp_f32_e32 v13, v13
	v_rcp_f32_e32 v8, v8
	v_rcp_f32_e32 v9, v9
	v_pk_mul_f32 v[4:5], v[70:71], v[38:39]
	v_mad_i64_i32 v[2:3], s[44:45], v14, s58, v[2:3]
	v_pk_mul_f32 v[4:5], v[4:5], v[8:9]
	v_pk_mul_f32 v[8:9], v[64:65], v[32:33]
	v_lshl_add_u64 v[0:1], v[2:3], 0, v[0:1]
	v_pk_mul_f32 v[8:9], v[8:9], v[10:11]
	v_pk_fma_f32 v[10:11], v[12:13], s[22:23], s[22:23] op_sel_hi:[1,0,0]
	v_rcp_f32_e32 v10, v10
	v_rcp_f32_e32 v11, v11
	v_cvt_pk_fp8_f32 v12, v6, v7
	v_cvt_pk_fp8_f32 v13, v8, v9
	v_pk_mul_f32 v[6:7], v[66:67], v[34:35]
	v_cvt_pk_fp8_f32 v12, v4, v5 op_sel:[0,0,1]
	v_pk_mul_f32 v[6:7], v[6:7], v[10:11]
	s_nop 0
	v_cvt_pk_fp8_f32 v13, v6, v7 op_sel:[0,0,1]
	global_store_dwordx2 v[0:1], v[12:13], off nt
	s_cbranch_vccnz .LBB0_863
	s_andn2_b64 vcc, exec, s[4:5]
	s_cbranch_vccnz .LBB0_862
	s_barrier
	s_branch .LBB0_862

; __device__ __forceinline__ unsigned cvt_pk4_fp8(float a, float b, float c, float d) { int w = 0; w = __builtin_amdgcn_cvt_pk_fp8_f32(a, b, w, false); w = __builtin_amdgcn_cvt_pk_fp8_f32(c, d, w, true); return (unsigned)w; }
; __device__ __forceinline__ unsigned cvt_pk_bf16(float lo, float hi) { unsigned r; asm volatile("v_cvt_pk_bf16_f32 %0, %1, %2" : "=v"(r) : "v"(lo), "v"(hi)); return r; }
; __device__ __forceinline__ f32x2p silu_mul2k(f32x2p ag, f32x2p au, float kt, float ci) { const f32x2p t = ag * kt; f32x2p e; e.x = __builtin_amdgcn_exp2f(t.x); e.y = __builtin_amdgcn_exp2f(t.y);
;     const f32x2p d = e * ci + ci; f32x2p r; r.x = __builtin_amdgcn_rcpf(d.x); r.y = __builtin_amdgcn_rcpf(d.y); return (ag * au) * r; }
;     __device__ __forceinline__ void operator()(const f32x4 (&acc)[2][2][4][2], const Unit& u, int wr, int wc, int fr, int fq) const {
;     ...
;             for (int m = 0; m < 4; ++m) { const size_t off = (size_t)(row0 + ai * HALF + m * 16) * ldc + col0;
;                 const f32x4 g0 = acc[ai][0][m][0], g1 = acc[ai][0][m][1], u0 = acc[ai][1][m][0], u1 = acc[ai][1][m][1];
;                 float v[8];
;                 { const f32x2p a = silu_mul2k((f32x2p){g0[0], g0[1]}, (f32x2p){u0[0], u0[1]}, kt, ci), b = silu_mul2k((f32x2p){g0[2], g0[3]}, (f32x2p){u0[2], u0[3]}, kt, ci), c = silu_mul2k((f32x2p){g1[0], g1[1]}, (f32x2p){u1[0], u1[1]}, kt, ci), d = silu_mul2k((f32x2p){g1[2], g1[3]}, (f32x2p){u1[2], u1[3]}, kt, ci);
;                   v[0] = a.x; v[1] = a.y; v[2] = b.x; v[3] = b.y; v[4] = c.x; v[5] = c.y; v[6] = d.x; v[7] = d.y; }
;                 if constexpr (FP8OUT) { typedef unsigned u32x2 __attribute__((ext_vector_type(2))); u32x2 w; w.x = cvt_pk4_fp8(v[0], v[1], v[2], v[3]); w.y = cvt_pk4_fp8(v[4], v[5], v[6], v[7]); __builtin_nontemporal_store(w, (u32x2*)((unsigned char*)O + off)); }
;                 else { u32x4 w; w.x = cvt_pk_bf16(v[0], v[1]); w.y = cvt_pk_bf16(v[2], v[3]); w.z = cvt_pk_bf16(v[4], v[5]); w.w = cvt_pk_bf16(v[6], v[7]); __builtin_nontemporal_store(w, (u32x4*)((bf16_t*)O + off)); } }
.LBB0_1764:
	v_pk_mul_f32 v[0:1], v[156:157], s[16:17] op_sel_hi:[1,0]
	v_pk_mul_f32 v[8:9], v[156:157], v[124:125]
	v_exp_f32_e32 v2, v0
	v_exp_f32_e32 v3, v1
	v_pk_mul_f32 v[10:11], v[152:153], s[16:17] op_sel_hi:[1,0]
	v_pk_mul_f32 v[12:13], v[154:155], s[16:17] op_sel_hi:[1,0]
	v_exp_f32_e32 v10, v10
	v_pk_fma_f32 v[2:3], v[2:3], s[22:23], s[22:23] op_sel_hi:[1,0,0]
	v_exp_f32_e32 v11, v11
	v_rcp_f32_e32 v2, v2
	v_rcp_f32_e32 v3, v3
	v_exp_f32_e32 v12, v12
	v_pk_fma_f32 v[10:11], v[10:11], s[22:23], s[22:23] op_sel_hi:[1,0,0]
	v_exp_f32_e32 v13, v13
	v_pk_mul_f32 v[2:3], v[8:9], v[2:3]
	v_pk_mul_f32 v[8:9], v[158:159], s[16:17] op_sel_hi:[1,0]
	v_rcp_f32_e32 v10, v10
	v_exp_f32_e32 v8, v8
	v_exp_f32_e32 v9, v9
	v_rcp_f32_e32 v11, v11
	v_pk_mul_f32 v[6:7], v[158:159], v[126:127]
	v_add_u32_e32 v4, s74, v182
	v_pk_fma_f32 v[8:9], v[8:9], s[22:23], s[22:23] op_sel_hi:[1,0,0]
	v_lshl_add_u32 v0, s67, 7, v184
	v_rcp_f32_e32 v8, v8
	v_rcp_f32_e32 v9, v9
	v_ashrrev_i32_e32 v1, 31, v0
	s_nop 15
	s_nop 15
	v_pk_mul_f32 v[14:15], v[146:147], s[16:17] op_sel_hi:[1,0]
	v_pk_mul_f32 v[6:7], v[6:7], v[8:9]
	v_pk_mul_f32 v[8:9], v[152:153], v[120:121]
	v_exp_f32_e32 v14, v14
	v_pk_mul_f32 v[8:9], v[8:9], v[10:11]
	v_pk_fma_f32 v[10:11], v[12:13], s[22:23], s[22:23] op_sel_hi:[1,0,0]
	v_cvt_pk_fp8_f32 v12, v2, v3
	v_rcp_f32_e32 v10, v10
	v_rcp_f32_e32 v11, v11
	v_cvt_pk_fp8_f32 v12, v6, v7 op_sel:[0,0,1]
	v_pk_mul_f32 v[6:7], v[148:149], s[16:17] op_sel_hi:[1,0]
	v_cvt_pk_fp8_f32 v13, v8, v9
	v_exp_f32_e32 v6, v6
	v_exp_f32_e32 v7, v7
	v_pk_mul_f32 v[2:3], v[154:155], v[122:123]
	v_exp_f32_e32 v15, v15
	v_pk_mul_f32 v[2:3], v[2:3], v[10:11]
	v_pk_fma_f32 v[6:7], v[6:7], s[22:23], s[22:23] op_sel_hi:[1,0,0]
	v_cvt_pk_fp8_f32 v13, v2, v3 op_sel:[0,0,1]
	v_rcp_f32_e32 v6, v6
	v_rcp_f32_e32 v7, v7
	v_mov_b64_e32 v[2:3], s[20:21]
	v_mad_i64_i32 v[8:9], s[38:39], v4, s64, v[2:3]
	v_pk_mul_f32 v[10:11], v[148:149], v[116:117]
	v_lshl_add_u64 v[8:9], v[8:9], 0, v[0:1]
	v_pk_mul_f32 v[6:7], v[10:11], v[6:7]
	v_pk_mul_f32 v[10:11], v[150:151], s[16:17] op_sel_hi:[1,0]
	global_store_dwordx2 v[8:9], v[12:13], off nt
	v_exp_f32_e32 v10, v10
	v_exp_f32_e32 v11, v11
	v_pk_mul_f32 v[12:13], v[144:145], s[16:17] op_sel_hi:[1,0]
	v_pk_mul_f32 v[8:9], v[150:151], v[118:119]
	v_exp_f32_e32 v12, v12
	v_exp_f32_e32 v13, v13
	v_pk_fma_f32 v[10:11], v[10:11], s[22:23], s[22:23] op_sel_hi:[1,0,0]
	v_add_u32_e32 v5, 16, v4
	v_rcp_f32_e32 v10, v10
	v_rcp_f32_e32 v11, v11
	v_pk_fma_f32 v[12:13], v[12:13], s[22:23], s[22:23] op_sel_hi:[1,0,0]
	s_andn2_b64 vcc, exec, s[4:5]
	v_rcp_f32_e32 v12, v12
	v_rcp_f32_e32 v13, v13
	v_pk_mul_f32 v[8:9], v[8:9], v[10:11]
	v_pk_mul_f32 v[10:11], v[144:145], v[112:113]
	s_mov_b64 s[4:5], -1
	v_pk_mul_f32 v[10:11], v[10:11], v[12:13]
	v_pk_fma_f32 v[12:13], v[14:15], s[22:23], s[22:23] op_sel_hi:[1,0,0]
	v_rcp_f32_e32 v12, v12
	v_rcp_f32_e32 v13, v13
	v_cvt_pk_fp8_f32 v15, v10, v11
	v_cvt_pk_fp8_f32 v14, v6, v7
	v_pk_mul_f32 v[6:7], v[146:147], v[114:115]
	v_pk_mul_f32 v[10:11], v[140:141], v[108:109]
	v_pk_mul_f32 v[6:7], v[6:7], v[12:13]
	v_pk_mul_f32 v[12:13], v[136:137], s[16:17] op_sel_hi:[1,0]
	v_cvt_pk_fp8_f32 v15, v6, v7 op_sel:[0,0,1]
	v_pk_mul_f32 v[6:7], v[140:141], s[16:17] op_sel_hi:[1,0]
	v_cvt_pk_fp8_f32 v14, v8, v9 op_sel:[0,0,1]
	v_exp_f32_e32 v6, v6
	v_exp_f32_e32 v7, v7
	v_exp_f32_e32 v12, v12
	v_exp_f32_e32 v13, v13
	v_mad_i64_i32 v[8:9], s[38:39], v5, s64, v[2:3]
	v_pk_fma_f32 v[6:7], v[6:7], s[22:23], s[22:23] op_sel_hi:[1,0,0]
	v_lshl_add_u64 v[8:9], v[8:9], 0, v[0:1]
	v_rcp_f32_e32 v6, v6
	v_rcp_f32_e32 v7, v7
	global_store_dwordx2 v[8:9], v[14:15], off nt
	v_pk_fma_f32 v[12:13], v[12:13], s[22:23], s[22:23] op_sel_hi:[1,0,0]
	v_pk_mul_f32 v[14:15], v[138:139], s[16:17] op_sel_hi:[1,0]
	v_pk_mul_f32 v[6:7], v[10:11], v[6:7]
	v_pk_mul_f32 v[10:11], v[142:143], s[16:17] op_sel_hi:[1,0]
	v_rcp_f32_e32 v12, v12
	v_exp_f32_e32 v10, v10
	v_exp_f32_e32 v11, v11
	v_rcp_f32_e32 v13, v13
	v_exp_f32_e32 v14, v14
	v_exp_f32_e32 v15, v15
	v_pk_fma_f32 v[10:11], v[10:11], s[22:23], s[22:23] op_sel_hi:[1,0,0]
	v_pk_mul_f32 v[8:9], v[142:143], v[110:111]
	v_rcp_f32_e32 v10, v10
	v_rcp_f32_e32 v11, v11
	v_add_u32_e32 v5, 32, v4
	v_pk_mul_f32 v[8:9], v[8:9], v[10:11]
	v_pk_mul_f32 v[10:11], v[136:137], v[104:105]
	s_nop 0
	v_pk_mul_f32 v[10:11], v[10:11], v[12:13]
	v_pk_fma_f32 v[12:13], v[14:15], s[22:23], s[22:23] op_sel_hi:[1,0,0]
	v_rcp_f32_e32 v12, v12
	v_rcp_f32_e32 v13, v13
	v_cvt_pk_fp8_f32 v15, v10, v11
	v_cvt_pk_fp8_f32 v14, v6, v7
	v_pk_mul_f32 v[6:7], v[138:139], v[106:107]
	v_pk_mul_f32 v[10:11], v[132:133], v[100:101]
	v_pk_mul_f32 v[6:7], v[6:7], v[12:13]
	v_pk_mul_f32 v[12:13], v[128:129], s[16:17] op_sel_hi:[1,0]
	v_cvt_pk_fp8_f32 v15, v6, v7 op_sel:[0,0,1]
	v_pk_mul_f32 v[6:7], v[132:133], s[16:17] op_sel_hi:[1,0]
	v_cvt_pk_fp8_f32 v14, v8, v9 op_sel:[0,0,1]
	v_exp_f32_e32 v6, v6
	v_exp_f32_e32 v7, v7
	v_exp_f32_e32 v12, v12
	v_exp_f32_e32 v13, v13
	v_mad_i64_i32 v[8:9], s[38:39], v5, s64, v[2:3]
	v_pk_fma_f32 v[6:7], v[6:7], s[22:23], s[22:23] op_sel_hi:[1,0,0]
	v_lshl_add_u64 v[8:9], v[8:9], 0, v[0:1]
	v_rcp_f32_e32 v6, v6
	v_rcp_f32_e32 v7, v7
	global_store_dwordx2 v[8:9], v[14:15], off nt
	v_pk_fma_f32 v[12:13], v[12:13], s[22:23], s[22:23] op_sel_hi:[1,0,0]
	v_pk_mul_f32 v[14:15], v[130:131], s[16:17] op_sel_hi:[1,0]
	v_pk_mul_f32 v[6:7], v[10:11], v[6:7]
	v_pk_mul_f32 v[10:11], v[134:135], s[16:17] op_sel_hi:[1,0]
	v_rcp_f32_e32 v12, v12
	v_exp_f32_e32 v10, v10
	v_exp_f32_e32 v11, v11
	v_rcp_f32_e32 v13, v13
	v_exp_f32_e32 v14, v14
	v_exp_f32_e32 v15, v15
	v_pk_fma_f32 v[10:11], v[10:11], s[22:23], s[22:23] op_sel_hi:[1,0,0]
; __device__ __forceinline__ unsigned cvt_pk4_fp8(float a, float b, float c, float d) { int w = 0; w = __builtin_amdgcn_cvt_pk_fp8_f32(a, b, w, false); w = __builtin_amdgcn_cvt_pk_fp8_f32(c, d, w, true); return (unsigned)w; }
;     __device__ __forceinline__ void operator()(const f32x4 (&acc)[2][2][4][2], const Unit& u, int wr, int wc, int fr, int fq) const {
;     ...
;             for (int m = 0; m < 4; ++m) { const size_t off = (size_t)(row0 + ai * HALF + m * 16) * ldc + col0;
;                 const f32x4 g0 = acc[ai][0][m][0], g1 = acc[ai][0][m][1], u0 = acc[ai][1][m][0], u1 = acc[ai][1][m][1];
;                 float v[8];
;                 { const f32x2p a = silu_mul2k((f32x2p){g0[0], g0[1]}, (f32x2p){u0[0], u0[1]}, kt, ci), b = silu_mul2k((f32x2p){g0[2], g0[3]}, (f32x2p){u0[2], u0[3]}, kt, ci), c = silu_mul2k((f32x2p){g1[0], g1[1]}, (f32x2p){u1[0], u1[1]}, kt, ci), d = silu_mul2k((f32x2p){g1[2], g1[3]}, (f32x2p){u1[2], u1[3]}, kt, ci);
;                   v[0] = a.x; v[1] = a.y; v[2] = b.x; v[3] = b.y; v[4] = c.x; v[5] = c.y; v[6] = d.x; v[7] = d.y; }
;                 if constexpr (FP8OUT) { typedef unsigned u32x2 __attribute__((ext_vector_type(2))); u32x2 w; w.x = cvt_pk4_fp8(v[0], v[1], v[2], v[3]); w.y = cvt_pk4_fp8(v[4], v[5], v[6], v[7]); __builtin_nontemporal_store(w, (u32x2*)((unsigned char*)O + off)); }
;                 else { u32x4 w; w.x = cvt_pk_bf16(v[0], v[1]); w.y = cvt_pk_bf16(v[2], v[3]); w.z = cvt_pk_bf16(v[4], v[5]); w.w = cvt_pk_bf16(v[6], v[7]); __builtin_nontemporal_store(w, (u32x4*)((bf16_t*)O + off)); } }
; template <class Epi, class Sched, bool ALIGN_EPI = false, bool SP2 = false, bool FP8 = false, bool PEEL = false>
; __device__ __forceinline__ void gemm_phase(PG8_LAS unsigned char* lds, const Gemm g, const Sched& S, const Epi& E, const int wid) {
;     ...
;         if constexpr (!Epi::AFTER_DRAIN) { E(acc, cur, wr, wc, fr, fq); S.done(cur); }
;         if (!has_next) break;
;         if constexpr (!PEEL) {
; #pragma unroll
;         for (int a = 0; a < 2; ++a)
; #pragma unroll
;             for (int b = 0; b < 2; ++b)
; #pragma unroll
;                 for (int m = 0; m < 4; ++m)
; #pragma unroll
;                     for (int n = 0; n < 2; ++n) acc[a][b][m][n] = (f32x4){0.f, 0.f, 0.f, 0.f};
;         }
;         cur = nxt; cA = nA; cB = nB; ++ui;
;         if constexpr (ALIGN_EPI) { if (wr == 1) PG8_BAR; }
	v_pk_mul_f32 v[8:9], v[134:135], v[102:103]
	v_rcp_f32_e32 v10, v10
	v_rcp_f32_e32 v11, v11
	v_add_u32_e32 v5, 48, v4
	v_pk_mul_f32 v[8:9], v[8:9], v[10:11]
	v_pk_mul_f32 v[10:11], v[128:129], v[96:97]
	s_nop 0
	v_pk_mul_f32 v[10:11], v[10:11], v[12:13]
	v_pk_fma_f32 v[12:13], v[14:15], s[22:23], s[22:23] op_sel_hi:[1,0,0]
	v_rcp_f32_e32 v12, v12
	v_rcp_f32_e32 v13, v13
	v_cvt_pk_fp8_f32 v15, v10, v11
	v_cvt_pk_fp8_f32 v14, v6, v7
	v_pk_mul_f32 v[6:7], v[130:131], v[98:99]
	v_pk_mul_f32 v[10:11], v[92:93], v[60:61]
	v_pk_mul_f32 v[6:7], v[6:7], v[12:13]
	v_pk_mul_f32 v[12:13], v[88:89], s[16:17] op_sel_hi:[1,0]
	v_cvt_pk_fp8_f32 v15, v6, v7 op_sel:[0,0,1]
	v_pk_mul_f32 v[6:7], v[92:93], s[16:17] op_sel_hi:[1,0]
	v_cvt_pk_fp8_f32 v14, v8, v9 op_sel:[0,0,1]
	v_exp_f32_e32 v6, v6
	v_exp_f32_e32 v7, v7
	v_exp_f32_e32 v12, v12
	v_exp_f32_e32 v13, v13
	v_mad_i64_i32 v[8:9], s[38:39], v5, s64, v[2:3]
	v_pk_fma_f32 v[6:7], v[6:7], s[22:23], s[22:23] op_sel_hi:[1,0,0]
	v_lshl_add_u64 v[8:9], v[8:9], 0, v[0:1]
	v_rcp_f32_e32 v6, v6
	v_rcp_f32_e32 v7, v7
	global_store_dwordx2 v[8:9], v[14:15], off nt
	v_pk_fma_f32 v[12:13], v[12:13], s[22:23], s[22:23] op_sel_hi:[1,0,0]
	v_pk_mul_f32 v[14:15], v[90:91], s[16:17] op_sel_hi:[1,0]
	v_pk_mul_f32 v[6:7], v[10:11], v[6:7]
	v_pk_mul_f32 v[10:11], v[94:95], s[16:17] op_sel_hi:[1,0]
	v_rcp_f32_e32 v12, v12
	v_exp_f32_e32 v10, v10
	v_exp_f32_e32 v11, v11
	v_rcp_f32_e32 v13, v13
	v_exp_f32_e32 v14, v14
	v_exp_f32_e32 v15, v15
	v_pk_fma_f32 v[10:11], v[10:11], s[22:23], s[22:23] op_sel_hi:[1,0,0]
	v_pk_mul_f32 v[8:9], v[94:95], v[62:63]
	v_rcp_f32_e32 v10, v10
	v_rcp_f32_e32 v11, v11
	v_add_u32_e32 v5, 0x80, v4
	v_pk_mul_f32 v[8:9], v[8:9], v[10:11]
	v_pk_mul_f32 v[10:11], v[88:89], v[56:57]
	s_nop 0
	v_pk_mul_f32 v[10:11], v[10:11], v[12:13]
	v_pk_fma_f32 v[12:13], v[14:15], s[22:23], s[22:23] op_sel_hi:[1,0,0]
	v_rcp_f32_e32 v12, v12
	v_rcp_f32_e32 v13, v13
	v_cvt_pk_fp8_f32 v15, v10, v11
	v_cvt_pk_fp8_f32 v14, v6, v7
	v_pk_mul_f32 v[6:7], v[90:91], v[58:59]
	v_pk_mul_f32 v[10:11], v[84:85], v[52:53]
	v_pk_mul_f32 v[6:7], v[6:7], v[12:13]
	v_pk_mul_f32 v[12:13], v[80:81], s[16:17] op_sel_hi:[1,0]
	v_cvt_pk_fp8_f32 v15, v6, v7 op_sel:[0,0,1]
	v_pk_mul_f32 v[6:7], v[84:85], s[16:17] op_sel_hi:[1,0]
	v_cvt_pk_fp8_f32 v14, v8, v9 op_sel:[0,0,1]
	v_exp_f32_e32 v6, v6
	v_exp_f32_e32 v7, v7
	v_exp_f32_e32 v12, v12
	v_exp_f32_e32 v13, v13
	v_mad_i64_i32 v[8:9], s[38:39], v5, s64, v[2:3]
	v_pk_fma_f32 v[6:7], v[6:7], s[22:23], s[22:23] op_sel_hi:[1,0,0]
	v_lshl_add_u64 v[8:9], v[8:9], 0, v[0:1]
	v_rcp_f32_e32 v6, v6
	v_rcp_f32_e32 v7, v7
	global_store_dwordx2 v[8:9], v[14:15], off nt
	v_pk_fma_f32 v[12:13], v[12:13], s[22:23], s[22:23] op_sel_hi:[1,0,0]
	v_pk_mul_f32 v[14:15], v[82:83], s[16:17] op_sel_hi:[1,0]
	v_pk_mul_f32 v[6:7], v[10:11], v[6:7]
	v_pk_mul_f32 v[10:11], v[86:87], s[16:17] op_sel_hi:[1,0]
	v_rcp_f32_e32 v12, v12
	v_exp_f32_e32 v10, v10
	v_exp_f32_e32 v11, v11
	v_rcp_f32_e32 v13, v13
	v_exp_f32_e32 v14, v14
	v_exp_f32_e32 v15, v15
	v_pk_fma_f32 v[10:11], v[10:11], s[22:23], s[22:23] op_sel_hi:[1,0,0]
	v_pk_mul_f32 v[8:9], v[86:87], v[54:55]
	v_rcp_f32_e32 v10, v10
	v_rcp_f32_e32 v11, v11
	v_add_u32_e32 v5, 0x90, v4
	v_pk_mul_f32 v[8:9], v[8:9], v[10:11]
	v_pk_mul_f32 v[10:11], v[80:81], v[48:49]
	s_nop 0
	v_pk_mul_f32 v[10:11], v[10:11], v[12:13]
	v_pk_fma_f32 v[12:13], v[14:15], s[22:23], s[22:23] op_sel_hi:[1,0,0]
	v_rcp_f32_e32 v12, v12
	v_rcp_f32_e32 v13, v13
	v_cvt_pk_fp8_f32 v15, v10, v11
	v_cvt_pk_fp8_f32 v14, v6, v7
	v_pk_mul_f32 v[6:7], v[82:83], v[50:51]
	v_pk_mul_f32 v[10:11], v[76:77], v[44:45]
	v_pk_mul_f32 v[6:7], v[6:7], v[12:13]
	v_pk_mul_f32 v[12:13], v[72:73], s[16:17] op_sel_hi:[1,0]
	v_cvt_pk_fp8_f32 v15, v6, v7 op_sel:[0,0,1]
	v_pk_mul_f32 v[6:7], v[76:77], s[16:17] op_sel_hi:[1,0]
	v_cvt_pk_fp8_f32 v14, v8, v9 op_sel:[0,0,1]
	v_exp_f32_e32 v6, v6
	v_exp_f32_e32 v7, v7
	v_exp_f32_e32 v12, v12
	v_exp_f32_e32 v13, v13
	v_mad_i64_i32 v[8:9], s[38:39], v5, s64, v[2:3]
	v_pk_fma_f32 v[6:7], v[6:7], s[22:23], s[22:23] op_sel_hi:[1,0,0]
	v_lshl_add_u64 v[8:9], v[8:9], 0, v[0:1]
	v_rcp_f32_e32 v6, v6
	v_rcp_f32_e32 v7, v7
	global_store_dwordx2 v[8:9], v[14:15], off nt
	v_pk_fma_f32 v[12:13], v[12:13], s[22:23], s[22:23] op_sel_hi:[1,0,0]
	v_pk_mul_f32 v[14:15], v[74:75], s[16:17] op_sel_hi:[1,0]
	v_pk_mul_f32 v[6:7], v[10:11], v[6:7]
	v_pk_mul_f32 v[10:11], v[78:79], s[16:17] op_sel_hi:[1,0]
	v_rcp_f32_e32 v12, v12
	v_exp_f32_e32 v10, v10
	v_exp_f32_e32 v11, v11
	v_rcp_f32_e32 v13, v13
	v_exp_f32_e32 v14, v14
	v_exp_f32_e32 v15, v15
	v_pk_fma_f32 v[10:11], v[10:11], s[22:23], s[22:23] op_sel_hi:[1,0,0]
	v_pk_mul_f32 v[8:9], v[78:79], v[46:47]
	v_rcp_f32_e32 v10, v10
	v_rcp_f32_e32 v11, v11
	v_add_u32_e32 v5, 0xa0, v4
	v_pk_mul_f32 v[8:9], v[8:9], v[10:11]
	v_pk_mul_f32 v[10:11], v[72:73], v[40:41]
	s_nop 0
	v_pk_mul_f32 v[10:11], v[10:11], v[12:13]
	v_pk_fma_f32 v[12:13], v[14:15], s[22:23], s[22:23] op_sel_hi:[1,0,0]
	v_rcp_f32_e32 v12, v12
	v_rcp_f32_e32 v13, v13
	v_cvt_pk_fp8_f32 v15, v10, v11
	v_cvt_pk_fp8_f32 v14, v6, v7
	v_pk_mul_f32 v[6:7], v[74:75], v[42:43]
	v_pk_mul_f32 v[10:11], v[64:65], s[16:17] op_sel_hi:[1,0]
	v_pk_mul_f32 v[6:7], v[6:7], v[12:13]
	v_cvt_pk_fp8_f32 v14, v8, v9 op_sel:[0,0,1]
	v_cvt_pk_fp8_f32 v15, v6, v7 op_sel:[0,0,1]
	v_pk_mul_f32 v[6:7], v[68:69], s[16:17] op_sel_hi:[1,0]
	v_mad_i64_i32 v[8:9], s[38:39], v5, s64, v[2:3]
	v_exp_f32_e32 v6, v6
	v_exp_f32_e32 v7, v7
	v_lshl_add_u64 v[8:9], v[8:9], 0, v[0:1]
	global_store_dwordx2 v[8:9], v[14:15], off nt
	v_pk_mul_f32 v[8:9], v[68:69], v[36:37]
	v_pk_fma_f32 v[6:7], v[6:7], s[22:23], s[22:23] op_sel_hi:[1,0,0]
	v_exp_f32_e32 v10, v10
	v_rcp_f32_e32 v6, v6
	v_rcp_f32_e32 v7, v7
	v_exp_f32_e32 v11, v11
	v_pk_mul_f32 v[12:13], v[66:67], s[16:17] op_sel_hi:[1,0]
	v_add_u32_e32 v14, 0xb0, v4
	v_pk_mul_f32 v[6:7], v[8:9], v[6:7]
	v_pk_mul_f32 v[8:9], v[70:71], s[16:17] op_sel_hi:[1,0]
	v_pk_fma_f32 v[10:11], v[10:11], s[22:23], s[22:23] op_sel_hi:[1,0,0]
	v_exp_f32_e32 v8, v8
	v_exp_f32_e32 v9, v9
	v_rcp_f32_e32 v10, v10
	v_rcp_f32_e32 v11, v11
	v_exp_f32_e32 v12, v12
	v_pk_fma_f32 v[8:9], v[8:9], s[22:23], s[22:23] op_sel_hi:[1,0,0]
	v_exp_f32_e32 v13, v13
	v_rcp_f32_e32 v8, v8
	v_rcp_f32_e32 v9, v9
	v_pk_mul_f32 v[4:5], v[70:71], v[38:39]
	v_mad_i64_i32 v[2:3], s[38:39], v14, s64, v[2:3]
	v_pk_mul_f32 v[4:5], v[4:5], v[8:9]
	v_pk_mul_f32 v[8:9], v[64:65], v[32:33]
	v_lshl_add_u64 v[0:1], v[2:3], 0, v[0:1]
	v_pk_mul_f32 v[8:9], v[8:9], v[10:11]
	v_pk_fma_f32 v[10:11], v[12:13], s[22:23], s[22:23] op_sel_hi:[1,0,0]
	v_rcp_f32_e32 v10, v10
	v_rcp_f32_e32 v11, v11
	v_cvt_pk_fp8_f32 v12, v6, v7
	v_cvt_pk_fp8_f32 v13, v8, v9
	v_pk_mul_f32 v[6:7], v[66:67], v[34:35]
	v_cvt_pk_fp8_f32 v12, v4, v5 op_sel:[0,0,1]
	v_pk_mul_f32 v[6:7], v[6:7], v[10:11]
	s_nop 0
	v_cvt_pk_fp8_f32 v13, v6, v7 op_sel:[0,0,1]
	global_store_dwordx2 v[0:1], v[12:13], off nt
	s_cbranch_vccnz .LBB0_1753
	s_andn2_b64 vcc, exec, s[6:7]
	s_cbranch_vccnz .LBB0_1752
	s_barrier
	s_branch .LBB0_1752
